# v034 + cross-wave combine: all 8 partial-O ds_read_b128 issued up front into free regs with counted waits
# speedup vs baseline: 1.0045x; 1.0045x over previous
.LBB3_141:
	s_mul_i32 s2, s41, 0x6000
	v_or_b32_e32 v98, s2, v206
	v_add_u32_e32 v250, 0x12000, v98
	ds_read_b128 v[98:101], v250 offset:8192
	v_cvt_pk_bf16_f32 v50, v50, v51
	v_cvt_pk_bf16_f32 v51, v52, v53
	v_cvt_pk_bf16_f32 v52, v54, v55
	v_cvt_pk_bf16_f32 v53, v56, v57
	ds_read_b128 v[54:57], v250 offset:9216
	v_cvt_pk_bf16_f32 v214, v82, v83
	v_cvt_pk_bf16_f32 v215, v84, v85
	ds_read_b128 v[82:85], v250 offset:13312
	s_waitcnt lgkmcnt(2)
	v_mfma_f32_32x32x16_bf16 v[114:129], v[98:101], v[50:53], 0
	ds_read_b128 v[98:101], v250 offset:12288
	v_cvt_pk_bf16_f32 v18, v18, v19
	v_cvt_pk_bf16_f32 v19, v20, v21
	v_cvt_pk_bf16_f32 v20, v22, v23
	v_cvt_pk_bf16_f32 v21, v24, v25
	v_cvt_pk_bf16_f32 v216, v86, v87
	v_cvt_pk_bf16_f32 v217, v88, v89
	v_cvt_pk_bf16_f32 v86, v10, v11
	s_waitcnt lgkmcnt(0)
	v_mfma_f32_32x32x16_bf16 v[98:113], v[98:101], v[50:53], 0
	v_cvt_pk_bf16_f32 v50, v58, v59
	v_cvt_pk_bf16_f32 v51, v60, v61
	v_cvt_pk_bf16_f32 v52, v62, v63
	v_cvt_pk_bf16_f32 v53, v64, v65
	ds_read_b128 v[58:61], v250 offset:10240
	v_cvt_pk_bf16_f32 v87, v12, v13
	v_cvt_pk_bf16_f32 v88, v14, v15
	v_mfma_f32_32x32x16_bf16 v[114:129], v[54:57], v[50:53], v[114:129]
	v_cvt_pk_bf16_f32 v2, v2, v3
	v_cvt_pk_bf16_f32 v3, v4, v5
	v_cvt_pk_bf16_f32 v4, v6, v7
	v_cvt_pk_bf16_f32 v5, v8, v9
	v_cvt_pk_bf16_f32 v6, v42, v43
	v_cvt_pk_bf16_f32 v7, v44, v45
	v_cvt_pk_bf16_f32 v8, v46, v47
	v_mfma_f32_32x32x16_bf16 v[98:113], v[82:85], v[50:53], v[98:113]
	ds_read_b128 v[22:25], v250 offset:14336
	ds_read_b128 v[50:53], v250 offset:11264
	ds_read_b128 v[10:13], v250
	v_cvt_pk_bf16_f32 v9, v48, v49
	v_cvt_pk_bf16_f32 v54, v90, v91
	v_cvt_pk_bf16_f32 v55, v92, v93
	v_cvt_pk_bf16_f32 v56, v94, v95
	v_cvt_pk_bf16_f32 v57, v96, v97
	s_waitcnt lgkmcnt(3)
	v_mfma_f32_32x32x16_bf16 v[114:129], v[58:61], v[18:21], v[114:129]
	v_cvt_pk_bf16_f32 v58, v34, v35
	v_cvt_pk_bf16_f32 v59, v36, v37
	ds_read_b128 v[34:37], v250 offset:15360
	v_cvt_pk_bf16_f32 v60, v38, v39
	v_cvt_pk_bf16_f32 v61, v40, v41
	v_cvt_pk_bf16_f32 v202, v66, v67
	v_cvt_pk_bf16_f32 v203, v68, v69
	s_waitcnt lgkmcnt(3)
	v_mfma_f32_32x32x16_bf16 v[98:113], v[22:25], v[18:21], v[98:113]
	v_cvt_pk_bf16_f32 v18, v26, v27
	v_cvt_pk_bf16_f32 v19, v28, v29
	v_cvt_pk_bf16_f32 v20, v30, v31
	v_cvt_pk_bf16_f32 v21, v32, v33
	v_cvt_pk_bf16_f32 v204, v70, v71
	v_cvt_pk_bf16_f32 v205, v72, v73
	v_cvt_pk_bf16_f32 v82, v74, v75
	s_waitcnt lgkmcnt(2)
	v_mfma_f32_32x32x16_bf16 v[114:129], v[50:53], v[18:21], v[114:129]
	v_cvt_pk_bf16_f32 v83, v76, v77
	v_cvt_pk_bf16_f32 v84, v78, v79
	v_cvt_pk_bf16_f32 v85, v80, v81
	s_lshl_b32 s2, s20, 6
	s_mov_b32 s41, 1
	s_mov_b64 s[20:21], 0
	s_nop 5
	v_max3_f32 v14, v114, s38, v115
	s_waitcnt lgkmcnt(0)
	v_mfma_f32_32x32x16_bf16 v[98:113], v[34:37], v[18:21], v[98:113]
	ds_read_b128 v[50:53], v250 offset:1024
	ds_read_b128 v[18:21], v250 offset:4096
	ds_read_b128 v[62:65], v250 offset:5120
	v_max3_f32 v14, v14, v116, v117
	v_max3_f32 v14, v14, v118, v119
	v_max3_f32 v14, v14, v120, v121
	v_max3_f32 v14, v14, v122, v123
	v_max3_f32 v14, v14, v124, v125
	v_max3_f32 v14, v14, v126, v127
	v_mfma_f32_32x32x16_bf16 v[34:49], v[214:217], v[10:13], 0
	v_max3_f32 v14, v14, v128, v129
	s_nop 0
	v_max3_f32 v14, v14, v98, v99
	v_max3_f32 v14, v14, v100, v101
	v_max3_f32 v14, v14, v102, v103
	v_max3_f32 v14, v14, v104, v105
	v_max3_f32 v14, v14, v106, v107
	v_max3_f32 v14, v14, v108, v109
	s_waitcnt lgkmcnt(1)
	v_mfma_f32_32x32x16_bf16 v[18:33], v[214:217], v[18:21], 0
	v_max3_f32 v14, v14, v110, v111
	v_max3_f32 v14, v14, v112, v113
	v_mov_b32_e32 v15, v14
	ds_read_b128 v[10:13], v250 offset:2048
	ds_read_b128 v[66:69], v250 offset:3072
	ds_read_b128 v[70:73], v250 offset:6144
	ds_read_b128 v[74:77], v250 offset:7168
	v_permlane32_swap_b32_e32 v14, v15
	v_max_f32_e32 v15, v15, v15
	v_mfma_f32_32x32x16_bf16 v[34:49], v[54:57], v[50:53], v[34:49]
	v_max_f32_e32 v14, v14, v14
	v_max_f32_e32 v14, v14, v15
	v_mul_f32_e32 v14, 0xbe38aa3b, v14
	v_fmamk_f32 v15, v114, 0x3e38aa3b, v14
	v_fmamk_f32 v50, v118, 0x3e38aa3b, v14
	v_exp_f32_e32 v50, v50
	v_fmamk_f32 v51, v119, 0x3e38aa3b, v14
	s_waitcnt lgkmcnt(4)
	v_mfma_f32_32x32x16_bf16 v[18:33], v[54:57], v[62:65], v[18:33]
	v_exp_f32_e32 v51, v51
	v_fmamk_f32 v52, v120, 0x3e38aa3b, v14
	v_exp_f32_e32 v52, v52
	v_fmamk_f32 v53, v121, 0x3e38aa3b, v14
	v_exp_f32_e32 v53, v53
	v_fmamk_f32 v109, v109, 0x3e38aa3b, v14
	s_waitcnt lgkmcnt(3)
	v_mfma_f32_32x32x16_bf16 v[34:49], v[58:61], v[10:13], v[34:49]
	v_exp_f32_e32 v10, v15
	v_fmamk_f32 v11, v115, 0x3e38aa3b, v14
	v_exp_f32_e32 v11, v11
	v_fmamk_f32 v12, v116, 0x3e38aa3b, v14
	v_exp_f32_e32 v12, v12
	v_fmamk_f32 v15, v117, 0x3e38aa3b, v14
	v_exp_f32_e32 v15, v15
	s_waitcnt lgkmcnt(1)
	v_mfma_f32_32x32x16_bf16 v[18:33], v[58:61], v[70:73], v[18:33]
	v_add_f32_e32 v13, 0, v10
	v_add_f32_e32 v13, v13, v11
	v_add_f32_e32 v13, v13, v12
	v_add_f32_e32 v13, v13, v15
	v_add_f32_e32 v13, v13, v50
	v_add_f32_e32 v13, v13, v51
	v_cvt_pk_bf16_f32 v10, v10, v11
	v_mfma_f32_32x32x16_bf16 v[34:49], v[6:9], v[66:69], v[34:49]
	v_cvt_pk_bf16_f32 v11, v12, v15
	v_cvt_pk_bf16_f32 v12, v50, v51
	s_waitcnt lgkmcnt(0)
	v_mfma_f32_32x32x16_bf16 v[18:33], v[6:9], v[74:77], v[18:33]
	v_fmamk_f32 v6, v122, 0x3e38aa3b, v14
	v_exp_f32_e32 v89, v6
	v_fmamk_f32 v6, v123, 0x3e38aa3b, v14
	v_exp_f32_e32 v94, v6
	v_fmamk_f32 v7, v124, 0x3e38aa3b, v14
	v_add_f32_e32 v6, v13, v52
	v_exp_f32_e32 v95, v7
	v_fmamk_f32 v7, v125, 0x3e38aa3b, v14
	v_add_f32_e32 v6, v6, v53
	v_exp_f32_e32 v96, v7
	v_fmamk_f32 v7, v126, 0x3e38aa3b, v14
	v_add_f32_e32 v6, v6, v89
	v_exp_f32_e32 v97, v7
	v_fmamk_f32 v7, v127, 0x3e38aa3b, v14
	v_add_f32_e32 v6, v6, v94
	v_exp_f32_e32 v114, v7
	v_fmamk_f32 v7, v128, 0x3e38aa3b, v14
	v_add_f32_e32 v6, v6, v95
	v_exp_f32_e32 v115, v7
	v_fmamk_f32 v7, v129, 0x3e38aa3b, v14
	v_add_f32_e32 v6, v6, v96
	v_exp_f32_e32 v116, v7
	v_fmamk_f32 v7, v98, 0x3e38aa3b, v14
	v_add_f32_e32 v6, v6, v97
	v_exp_f32_e32 v98, v7
	v_fmamk_f32 v7, v99, 0x3e38aa3b, v14
	v_add_f32_e32 v6, v6, v114
	v_exp_f32_e32 v99, v7
	v_fmamk_f32 v7, v100, 0x3e38aa3b, v14
	v_add_f32_e32 v6, v6, v115
	v_exp_f32_e32 v100, v7
	v_fmamk_f32 v7, v101, 0x3e38aa3b, v14
	v_add_f32_e32 v6, v6, v116
	v_exp_f32_e32 v101, v7
	v_fmamk_f32 v7, v102, 0x3e38aa3b, v14
	v_add_f32_e32 v6, v6, v98
	v_exp_f32_e32 v102, v7
	v_fmamk_f32 v7, v103, 0x3e38aa3b, v14
	v_add_f32_e32 v6, v6, v99
	v_exp_f32_e32 v103, v7
	v_add_f32_e32 v6, v6, v100
	v_add_f32_e32 v6, v6, v101
	v_add_f32_e32 v6, v6, v102
	v_add_f32_e32 v54, v6, v103
	v_fmamk_f32 v6, v104, 0x3e38aa3b, v14
	v_exp_f32_e32 v104, v6
	ds_read_b128 v[6:9], v250 offset:16384
	v_fmamk_f32 v13, v105, 0x3e38aa3b, v14
	v_exp_f32_e32 v105, v13
	v_cvt_pk_bf16_f32 v13, v52, v53
	ds_read_b128 v[50:53], v250 offset:18432
	ds_read_b128 v[90:93], v250 offset:17408
	s_waitcnt lgkmcnt(2)
	v_mfma_f32_32x32x16_bf16 v[66:81], v[6:9], v[10:13], 0
	v_add_f32_e32 v6, v54, v104
	v_add_f32_e32 v15, v6, v105
	v_fmamk_f32 v6, v106, 0x3e38aa3b, v14
	v_exp_f32_e32 v106, v6
	v_fmamk_f32 v6, v107, 0x3e38aa3b, v14
	v_exp_f32_e32 v107, v6
	ds_read_b128 v[6:9], v250 offset:19456
	s_waitcnt lgkmcnt(2)
	v_mfma_f32_32x32x16_bf16 v[50:65], v[50:53], v[10:13], 0
	v_fmamk_f32 v10, v108, 0x3e38aa3b, v14
	v_exp_f32_e32 v108, v10
	v_cvt_pk_bf16_f32 v10, v89, v94
	v_cvt_pk_bf16_f32 v11, v95, v96
	v_cvt_pk_bf16_f32 v12, v97, v114
	v_cvt_pk_bf16_f32 v13, v115, v116
	v_fmamk_f32 v94, v110, 0x3e38aa3b, v14
	v_exp_f32_e32 v89, v109
	s_waitcnt lgkmcnt(1)
	v_mfma_f32_32x32x16_bf16 v[66:81], v[90:93], v[10:13], v[66:81]
	ds_read_b128 v[90:93], v250 offset:20480
	v_exp_f32_e32 v109, v94
	v_add_f32_e32 v15, v15, v106
	v_add_f32_e32 v15, v15, v107
	v_add_f32_e32 v15, v15, v108
	v_add_f32_e32 v15, v15, v89
	v_add_f32_e32 v15, v15, v109
	s_waitcnt lgkmcnt(1)
	v_mfma_f32_32x32x16_bf16 v[50:65], v[6:9], v[10:13], v[50:65]
	v_cvt_pk_bf16_f32 v6, v98, v99
	v_cvt_pk_bf16_f32 v7, v100, v101
	v_cvt_pk_bf16_f32 v8, v102, v103
	v_cvt_pk_bf16_f32 v9, v104, v105
	ds_read_b128 v[10:13], v250 offset:22528
	ds_read_b128 v[94:97], v250 offset:21504
	s_waitcnt lgkmcnt(2)
	v_mfma_f32_32x32x16_bf16 v[66:81], v[90:93], v[6:9], v[66:81]
	v_fmamk_f32 v90, v111, 0x3e38aa3b, v14
	v_exp_f32_e32 v98, v90
	v_fmamk_f32 v90, v112, 0x3e38aa3b, v14
	v_fmac_f32_e32 v14, 0x3e38aa3b, v113
	v_exp_f32_e32 v99, v90
	ds_read_b128 v[90:93], v250 offset:23552
	v_add_f32_e32 v15, v15, v98
	s_waitcnt lgkmcnt(2)
	v_mfma_f32_32x32x16_bf16 v[50:65], v[10:13], v[6:9], v[50:65]
	v_exp_f32_e32 v11, v14
	v_add_f32_e32 v10, v15, v99
	v_cvt_pk_bf16_f32 v6, v106, v107
	v_cvt_pk_bf16_f32 v7, v108, v89
	v_cvt_pk_bf16_f32 v8, v109, v98
	v_cvt_pk_bf16_f32 v9, v99, v11
	v_add_f32_e32 v10, v10, v11
	v_mov_b32_e32 v11, v10
	s_waitcnt lgkmcnt(1)
	v_mfma_f32_32x32x16_bf16 v[66:81], v[94:97], v[6:9], v[66:81]
	v_permlane32_swap_b32_e32 v10, v11
	v_add_f32_e32 v10, v10, v11
	v_rcp_f32_e32 v101, v10
	v_cvt_pk_bf16_f32 v89, v16, v17
	v_ashrrev_i32_e32 v118, 3, v210
	v_and_b32_e32 v118, 0xffffffe0, v118
	v_bfe_u32 v119, v210, 6, 1
	v_add_u32_e32 v118, s16, v118
	v_lshl_or_b32 v118, v119, 4, v118
	v_or_b32_e32 v118, v118, v211
	v_lshlrev_b32_e32 v118, 10, v118
	v_add_u32_e32 v118, s2, v118
	v_bfe_u32 v119, v210, 7, 1
	v_lshl_or_b32 v118, v119, 5, v118
	v_or_b32_e32 v118, v118, v1
	v_lshlrev_b32_e32 v118, 2, v118
	global_load_dword v110, v118, s[12:13]
	global_load_dword v111, v118, s[72:73] offset:-4096
	global_load_dword v112, v118, s[72:73]
	global_load_dword v113, v118, s[76:77] offset:-4096
	global_load_dword v114, v118, s[76:77]
	global_load_dword v115, v118, s[78:79] offset:-4096
	global_load_dword v116, v118, s[78:79]
	global_load_dword v117, v118, s[74:75]
	s_nop 6
	s_waitcnt vmcnt(32)
	v_fmac_f32_e32 v245, v101, v70
	s_waitcnt lgkmcnt(0)
	v_mfma_f32_32x32x16_bf16 v[50:65], v[90:93], v[6:9], v[50:65]
	v_fmac_f32_e32 v243, v101, v71
	v_fmac_f32_e32 v241, v101, v72
	v_fmac_f32_e32 v239, v101, v73
	global_store_dword v252, v245, s[58:59] nt
	global_store_dword v252, v243, s[58:59] offset:1024 nt
	global_store_dword v252, v241, s[58:59] offset:2048 nt
	global_store_dword v252, v239, s[58:59] offset:3072 nt
	v_max3_f32 v6, v34, s38, v35
	v_max3_f32 v6, v6, v36, v37
	v_max3_f32 v6, v6, v38, v39
	v_max3_f32 v6, v6, v40, v41
	v_max3_f32 v7, v18, s38, v19
	v_max3_f32 v6, v6, v42, v43
	v_max3_f32 v7, v7, v20, v21
	v_max3_f32 v6, v6, v44, v45
	v_max3_f32 v7, v7, v22, v23
	v_max3_f32 v6, v6, v46, v47
	v_max3_f32 v7, v7, v24, v25
	v_max3_f32 v6, v6, v48, v49
	v_max3_f32 v7, v7, v26, v27
	v_max3_f32 v7, v7, v28, v29
	v_mov_b32_e32 v8, v6
	s_waitcnt vmcnt(32)
	v_fmac_f32_e32 v244, v101, v74
	v_fmac_f32_e32 v242, v101, v75
	v_fmac_f32_e32 v240, v101, v76
	v_fmac_f32_e32 v238, v101, v77
	global_store_dword v252, v244, s[60:61] nt
	global_store_dword v252, v242, s[60:61] offset:1024 nt
	global_store_dword v252, v240, s[60:61] offset:2048 nt
	global_store_dword v252, v238, s[60:61] offset:3072 nt
	v_max3_f32 v7, v7, v30, v31
	s_nop 0
	v_permlane32_swap_b32_e32 v6, v8
	v_max3_f32 v7, v7, v32, v33
	v_max_f32_e32 v8, v8, v8
	v_max_f32_e32 v6, v6, v6
	v_max_f32_e32 v90, v6, v8
	v_mov_b32_e32 v6, v7
	s_nop 1
	v_permlane32_swap_b32_e32 v7, v6
	v_mul_f32_e32 v8, 0xbe38aa3b, v90
	v_fmamk_f32 v9, v34, 0x3e38aa3b, v8
	v_max_f32_e32 v6, v6, v6
	v_max_f32_e32 v7, v7, v7
	v_exp_f32_e32 v9, v9
	s_waitcnt vmcnt(30)
	v_fmac_f32_e32 v236, v101, v78
	v_fmac_f32_e32 v234, v101, v79
	v_fmac_f32_e32 v232, v101, v80
	v_fmac_f32_e32 v230, v101, v81
	global_store_dword v252, v236, s[62:63] nt
	global_store_dword v252, v234, s[62:63] offset:1024 nt
	global_store_dword v252, v232, s[62:63] offset:2048 nt
	global_store_dword v252, v230, s[62:63] offset:3072 nt
	v_max_f32_e32 v91, v7, v6
	v_fmamk_f32 v7, v35, 0x3e38aa3b, v8
	v_exp_f32_e32 v7, v7
	v_fmamk_f32 v10, v36, 0x3e38aa3b, v8
	v_exp_f32_e32 v10, v10
	v_fmamk_f32 v11, v37, 0x3e38aa3b, v8
	v_exp_f32_e32 v11, v11
	v_fmamk_f32 v12, v38, 0x3e38aa3b, v8
	v_add_f32_e32 v6, 0, v9
	v_exp_f32_e32 v12, v12
	v_fmamk_f32 v13, v39, 0x3e38aa3b, v8
	v_add_f32_e32 v6, v6, v7
	v_exp_f32_e32 v13, v13
	v_fmamk_f32 v14, v40, 0x3e38aa3b, v8
	v_add_f32_e32 v6, v6, v10
	s_waitcnt vmcnt(32)
	v_fmac_f32_e32 v237, v101, v50
	v_fmac_f32_e32 v235, v101, v51
	v_fmac_f32_e32 v233, v101, v52
	v_fmac_f32_e32 v231, v101, v53
	global_store_dword v252, v237, s[64:65] nt
	global_store_dword v252, v235, s[64:65] offset:1024 nt
	global_store_dword v252, v233, s[64:65] offset:2048 nt
	global_store_dword v252, v231, s[64:65] offset:3072 nt
	v_exp_f32_e32 v14, v14
	v_fmamk_f32 v15, v41, 0x3e38aa3b, v8
	v_fmamk_f32 v16, v42, 0x3e38aa3b, v8
	v_add_f32_e32 v6, v6, v11
	v_exp_f32_e32 v15, v15
	v_exp_f32_e32 v92, v16
	v_fmamk_f32 v16, v43, 0x3e38aa3b, v8
	v_add_f32_e32 v6, v6, v12
	v_exp_f32_e32 v93, v16
	v_fmamk_f32 v16, v44, 0x3e38aa3b, v8
	v_add_f32_e32 v6, v6, v13
	v_exp_f32_e32 v94, v16
	v_fmamk_f32 v16, v45, 0x3e38aa3b, v8
	v_add_f32_e32 v6, v6, v14
	v_exp_f32_e32 v95, v16
	s_waitcnt vmcnt(32)
	v_fmac_f32_e32 v228, v101, v54
	v_fmac_f32_e32 v226, v101, v55
	v_fmac_f32_e32 v224, v101, v56
	v_fmac_f32_e32 v222, v101, v57
	global_store_dword v252, v228, s[66:67] nt
	global_store_dword v252, v226, s[66:67] offset:1024 nt
	global_store_dword v252, v224, s[66:67] offset:2048 nt
	global_store_dword v252, v222, s[66:67] offset:3072 nt
	v_fmamk_f32 v16, v46, 0x3e38aa3b, v8
	v_add_f32_e32 v6, v6, v15
	v_exp_f32_e32 v96, v16
	v_fmamk_f32 v16, v47, 0x3e38aa3b, v8
	v_add_f32_e32 v6, v6, v92
	v_exp_f32_e32 v97, v16
	v_fmamk_f32 v16, v48, 0x3e38aa3b, v8
	v_add_f32_e32 v6, v6, v93
	v_exp_f32_e32 v98, v16
	v_fmac_f32_e32 v8, 0x3e38aa3b, v49
	v_mul_f32_e32 v16, 0xbe38aa3b, v91
	v_add_f32_e32 v6, v6, v94
	v_exp_f32_e32 v99, v8
	v_fmamk_f32 v8, v18, 0x3e38aa3b, v16
	v_add_f32_e32 v6, v6, v95
	v_fmac_f32_e32 v249, v101, v66
	v_fmac_f32_e32 v248, v101, v67
	v_fmac_f32_e32 v247, v101, v68
	v_fmac_f32_e32 v246, v101, v69
	global_store_dword v252, v249, s[4:5] nt
	global_store_dword v252, v248, s[4:5] offset:1024 nt
	global_store_dword v252, v247, s[4:5] offset:2048 nt
	global_store_dword v252, v246, s[4:5] offset:3072 nt
	v_exp_f32_e32 v17, v8
	v_fmamk_f32 v8, v19, 0x3e38aa3b, v16
	v_add_f32_e32 v6, v6, v96
	v_exp_f32_e32 v18, v8
	v_fmamk_f32 v8, v20, 0x3e38aa3b, v16
	v_add_f32_e32 v6, v6, v97
	v_exp_f32_e32 v19, v8
	v_fmamk_f32 v8, v21, 0x3e38aa3b, v16
	v_add_f32_e32 v6, v6, v98
	v_exp_f32_e32 v20, v8
	v_fmamk_f32 v8, v22, 0x3e38aa3b, v16
	v_add_f32_e32 v100, v6, v99
	v_add_f32_e32 v6, 0, v17
	v_exp_f32_e32 v21, v8
	s_waitcnt vmcnt(32)
	v_fmac_f32_e32 v221, v101, v62
	v_fmac_f32_e32 v220, v101, v63
	v_fmac_f32_e32 v219, v101, v64
	v_fmac_f32_e32 v218, v101, v65
	global_store_dword v252, v221, s[70:71] nt
	global_store_dword v252, v220, s[70:71] offset:1024 nt
	global_store_dword v252, v219, s[70:71] offset:2048 nt
	global_store_dword v252, v218, s[70:71] offset:3072 nt
	v_fmamk_f32 v8, v23, 0x3e38aa3b, v16
	v_add_f32_e32 v6, v6, v18
	v_exp_f32_e32 v22, v8
	v_fmamk_f32 v8, v24, 0x3e38aa3b, v16
	v_add_f32_e32 v6, v6, v19
	v_exp_f32_e32 v23, v8
	v_fmamk_f32 v8, v25, 0x3e38aa3b, v16
	v_add_f32_e32 v6, v6, v20
	v_exp_f32_e32 v24, v8
	v_fmamk_f32 v8, v26, 0x3e38aa3b, v16
	v_add_f32_e32 v6, v6, v21
	v_exp_f32_e32 v25, v8
	v_add_f32_e32 v6, v6, v22
	v_add_f32_e32 v6, v6, v23
	v_fmac_f32_e32 v229, v101, v58
	v_fmac_f32_e32 v227, v101, v59
	v_fmac_f32_e32 v225, v101, v60
	v_fmac_f32_e32 v223, v101, v61
	global_store_dword v252, v229, s[68:69] nt
	global_store_dword v252, v227, s[68:69] offset:1024 nt
	global_store_dword v252, v225, s[68:69] offset:2048 nt
	global_store_dword v252, v223, s[68:69] offset:3072 nt
	v_add_f32_e32 v6, v6, v24
	v_add_f32_e32 v26, v6, v25
	v_fmamk_f32 v6, v27, 0x3e38aa3b, v16
	v_exp_f32_e32 v27, v6
	v_cvt_pk_bf16_f32 v6, v9, v7
	v_cvt_pk_bf16_f32 v7, v10, v11
	v_fmamk_f32 v10, v28, 0x3e38aa3b, v16
	v_cvt_pk_bf16_f32 v9, v14, v15
	v_exp_f32_e32 v28, v10
	v_fmamk_f32 v14, v29, 0x3e38aa3b, v16
	v_cvt_pk_bf16_f32 v8, v12, v13
	v_cvt_pk_bf16_f32 v13, v23, v24
	v_exp_f32_e32 v23, v14
	v_fmamk_f32 v14, v30, 0x3e38aa3b, v16
	v_mfma_f32_32x32x16_bf16 v[66:81], v[202:205], v[6:9], 0
	v_exp_f32_e32 v24, v14
	v_add_f32_e32 v14, v26, v27
	v_add_f32_e32 v14, v14, v28
	v_add_f32_e32 v14, v14, v23
	v_cvt_pk_bf16_f32 v10, v17, v18
	v_cvt_pk_bf16_f32 v11, v19, v20
	v_cvt_pk_bf16_f32 v12, v21, v22
	v_mfma_f32_32x32x16_bf16 v[34:49], v[2:5], v[6:9], 0
	v_fmamk_f32 v6, v31, 0x3e38aa3b, v16
	v_exp_f32_e32 v26, v6
	v_add_f32_e32 v14, v14, v24
	v_fmamk_f32 v6, v32, 0x3e38aa3b, v16
	v_fmac_f32_e32 v16, 0x3e38aa3b, v33
	v_exp_f32_e32 v29, v6
	v_exp_f32_e32 v30, v16
	v_mfma_f32_32x32x16_bf16 v[50:65], v[202:205], v[10:13], 0
	v_add_f32_e32 v18, v14, v26
	v_mov_b32_e32 v22, v100
	s_nop 1
	v_permlane32_swap_b32_e32 v100, v22
	v_add_f32_e32 v32, v100, v22
	v_cvt_pk_bf16_f32 v22, v25, v27
	v_cvt_pk_bf16_f32 v23, v28, v23
	v_mfma_f32_32x32x16_bf16 v[2:17], v[2:5], v[10:13], 0
	v_cvt_pk_bf16_f32 v24, v24, v26
	v_cvt_pk_bf16_f32 v25, v29, v30
	v_lshlrev_b32_e32 v26, 2, v213
	v_lshl_or_b32 v27, v212, 10, v26
	v_add_f32_e32 v18, v18, v29
	v_add_u32_e32 v28, 0x10000, v27
	v_add_f32_e32 v31, v18, v30
	v_mfma_f32_32x32x16_bf16 v[2:17], v[86:89], v[22:25], v[2:17]
	ds_write_b32 v28, v90
	v_add_u32_e32 v28, 0x10100, v27
	v_cvt_pk_bf16_f32 v18, v92, v93
	v_cvt_pk_bf16_f32 v19, v94, v95
	v_cvt_pk_bf16_f32 v20, v96, v97
	v_cvt_pk_bf16_f32 v21, v98, v99
	ds_write_b32 v28, v32
	v_mov_b32_e32 v28, v31
	v_mfma_f32_32x32x16_bf16 v[66:81], v[82:85], v[18:21], v[66:81]
	s_nop 0
	v_permlane32_swap_b32_e32 v31, v28
	s_nop 0
	v_cvt_pk_bf16_f32 v2, v2, v3
	v_cvt_pk_bf16_f32 v3, v4, v5
	v_cvt_pk_bf16_f32 v4, v6, v7
	v_cvt_pk_bf16_f32 v5, v8, v9
	v_mfma_f32_32x32x16_bf16 v[34:49], v[86:89], v[18:21], v[34:49]
	v_add_u32_e32 v19, 0x10200, v27
	v_add_f32_e32 v18, v31, v28
	ds_write_b32 v19, v91
	v_add_u32_e32 v19, 0x10300, v27
	ds_write_b32 v19, v18
	v_cvt_pk_bf16_f32 v18, v66, v67
	v_cvt_pk_bf16_f32 v19, v68, v69
	v_mfma_f32_32x32x16_bf16 v[50:65], v[82:85], v[22:25], v[50:65]
	v_lshl_or_b32 v22, v212, 13, v206
	ds_write_b128 v22, v[2:5] offset:6144
	v_cvt_pk_bf16_f32 v2, v10, v11
	v_cvt_pk_bf16_f32 v3, v12, v13
	v_cvt_pk_bf16_f32 v4, v14, v15
	v_cvt_pk_bf16_f32 v5, v16, v17
	ds_write_b128 v22, v[2:5] offset:7168
	v_bfe_u32 v16, v210, 6, 1
	v_ashrrev_i32_e32 v14, 7, v210
	v_and_b32_e32 v15, 1, v14
	v_cvt_pk_bf16_f32 v20, v70, v71
	v_cvt_pk_bf16_f32 v21, v72, v73
	ds_write_b128 v22, v[18:21]
	v_cvt_pk_bf16_f32 v18, v74, v75
	v_cvt_pk_bf16_f32 v19, v76, v77
	v_cvt_pk_bf16_f32 v20, v78, v79
	v_cvt_pk_bf16_f32 v21, v80, v81
	ds_write_b128 v22, v[18:21] offset:1024
	v_cvt_pk_bf16_f32 v18, v50, v51
	v_cvt_pk_bf16_f32 v19, v52, v53
	v_cvt_pk_bf16_f32 v20, v54, v55
	v_cvt_pk_bf16_f32 v21, v56, v57
	ds_write_b128 v22, v[18:21] offset:2048
	v_cvt_pk_bf16_f32 v18, v58, v59
	v_cvt_pk_bf16_f32 v19, v60, v61
	v_cvt_pk_bf16_f32 v20, v62, v63
	v_cvt_pk_bf16_f32 v21, v64, v65
	ds_write_b128 v22, v[18:21] offset:3072
	v_cvt_pk_bf16_f32 v18, v34, v35
	v_cvt_pk_bf16_f32 v19, v36, v37
	v_cvt_pk_bf16_f32 v20, v38, v39
	v_cvt_pk_bf16_f32 v21, v40, v41
	ds_write_b128 v22, v[18:21] offset:4096
	v_cvt_pk_bf16_f32 v18, v42, v43
	v_cvt_pk_bf16_f32 v19, v44, v45
	v_cvt_pk_bf16_f32 v20, v46, v47
	v_cvt_pk_bf16_f32 v21, v48, v49
	ds_write_b128 v22, v[18:21] offset:5120
	v_lshl_or_b32 v4, v15, 9, v26
	v_or_b32_e32 v5, 0x10000, v4
	v_or_b32_e32 v12, 0x10d00, v4
	s_waitcnt lgkmcnt(0)
	s_barrier
	v_or_b32_e32 v6, 0x10100, v4
	v_or_b32_e32 v7, 0x10400, v4
	v_or_b32_e32 v8, 0x10500, v4
	v_or_b32_e32 v9, 0x10800, v4
	v_or_b32_e32 v10, 0x10900, v4
	v_or_b32_e32 v11, 0x10c00, v4
	ds_read_b32 v5, v5
	ds_read_b32 v13, v6
	ds_read_b32 v15, v7
	ds_read_b32 v24, v8
	ds_read_b32 v25, v9
	ds_read_b32 v26, v10
	ds_read_b32 v27, v11
	ds_read_b32 v12, v12
	v_or_b32_e32 v6, 0x11000, v4
	v_or_b32_e32 v7, 0x11100, v4
	v_or_b32_e32 v8, 0x11400, v4
	v_or_b32_e32 v9, 0x11500, v4
	v_or_b32_e32 v10, 0x11800, v4
	v_or_b32_e32 v11, 0x11900, v4
	v_or_b32_e32 v28, 0x11c00, v4
	v_or_b32_e32 v4, 0x11d00, v4
	ds_read_b32 v29, v6
	ds_read_b32 v30, v7
	ds_read_b32 v31, v8
	ds_read_b32 v32, v9
	ds_read_b32 v33, v10
	ds_read_b32 v34, v11
	ds_read_b32 v28, v28
	ds_read_b32 v35, v4
	v_lshlrev_b32_e32 v44, 11, v14
	v_lshlrev_b32_e32 v45, 10, v16
	v_or3_b32 v44, v206, v44, v45
	ds_read_b128 v[48:51], v44
	ds_read_b128 v[52:55], v44 offset:8192
	ds_read_b128 v[56:59], v44 offset:16384
	ds_read_b128 v[60:63], v44 offset:24576
	ds_read_b128 v[64:67], v44 offset:32768
	ds_read_b128 v[68:71], v44 offset:40960
	ds_read_b128 v[72:75], v44 offset:49152
	ds_read_b128 v[76:79], v44 offset:57344
	s_waitcnt lgkmcnt(8)
	v_max_f32_e32 v4, v15, v15
	v_max_f32_e32 v6, v5, v5
	v_max_f32_e32 v4, v6, v4
	v_max3_f32 v4, v4, v25, v27
	v_max3_f32 v4, v4, v29, v31
	v_max3_f32 v36, v4, v33, v28
	v_sub_f32_e32 v4, v5, v36
	v_mul_f32_e32 v4, 0x3e38aa3b, v4
	v_exp_f32_e32 v37, v4
	s_nop 0
	v_fma_f32 v13, v13, v37, 0
	s_waitcnt lgkmcnt(7)
	v_lshlrev_b32_e32 v16, 16, v48
	v_and_b32_e32 v4, 0xffff0000, v48
	v_fma_f32 v38, v37, v4, 0
	v_lshlrev_b32_e32 v4, 16, v49
	v_fma_f32 v39, v37, v4, 0
	v_and_b32_e32 v4, 0xffff0000, v49
	v_sub_f32_e32 v5, v15, v36
	v_fma_f32 v40, v37, v4, 0
	v_lshlrev_b32_e32 v4, 16, v50
	v_mul_f32_e32 v5, 0x3e38aa3b, v5
	v_fma_f32 v41, v37, v4, 0
	v_and_b32_e32 v4, 0xffff0000, v50
	v_exp_f32_e32 v15, v5
	v_fma_f32 v42, v37, v4, 0
	v_lshlrev_b32_e32 v4, 16, v51
	v_fma_f32 v43, v37, v4, 0
	v_and_b32_e32 v4, 0xffff0000, v51
	v_fma_f32 v16, v37, v16, 0
	v_fma_f32 v37, v37, v4, 0
	s_waitcnt lgkmcnt(6)
	v_lshlrev_b32_e32 v4, 16, v52
	v_fmac_f32_e32 v16, v15, v4
	v_and_b32_e32 v4, 0xffff0000, v52
	v_fmac_f32_e32 v38, v15, v4
	v_lshlrev_b32_e32 v4, 16, v53
	v_fmac_f32_e32 v39, v15, v4
	v_and_b32_e32 v4, 0xffff0000, v53
	v_fmac_f32_e32 v40, v15, v4
	v_lshlrev_b32_e32 v4, 16, v54
	v_fmac_f32_e32 v41, v15, v4
	v_and_b32_e32 v4, 0xffff0000, v54
	v_fmac_f32_e32 v42, v15, v4
	v_lshlrev_b32_e32 v4, 16, v55
	v_fmac_f32_e32 v43, v15, v4
	v_sub_f32_e32 v4, v25, v36
	v_mul_f32_e32 v4, 0x3e38aa3b, v4
	v_fmac_f32_e32 v13, v24, v15
	v_exp_f32_e32 v24, v4
	v_and_b32_e32 v8, 0xffff0000, v55
	v_fmac_f32_e32 v37, v15, v8
	v_fmac_f32_e32 v13, v26, v24
	s_waitcnt lgkmcnt(5)
	v_lshlrev_b32_e32 v15, 16, v56
	v_and_b32_e32 v4, 0xffff0000, v56
	v_fmac_f32_e32 v38, v24, v4
	v_lshlrev_b32_e32 v4, 16, v57
	v_fmac_f32_e32 v39, v24, v4
	v_and_b32_e32 v4, 0xffff0000, v57
	v_sub_f32_e32 v5, v27, v36
	v_fmac_f32_e32 v40, v24, v4
	v_lshlrev_b32_e32 v4, 16, v58
	v_mul_f32_e32 v5, 0x3e38aa3b, v5
	v_fmac_f32_e32 v16, v24, v15
	v_fmac_f32_e32 v41, v24, v4
	v_and_b32_e32 v4, 0xffff0000, v58
	v_exp_f32_e32 v15, v5
	v_fmac_f32_e32 v42, v24, v4
	v_lshlrev_b32_e32 v4, 16, v59
	v_fmac_f32_e32 v43, v24, v4
	v_and_b32_e32 v4, 0xffff0000, v59
	v_fmac_f32_e32 v37, v24, v4
	s_waitcnt lgkmcnt(4)
	v_lshlrev_b32_e32 v4, 16, v60
	v_fmac_f32_e32 v16, v15, v4
	v_and_b32_e32 v4, 0xffff0000, v60
	v_fmac_f32_e32 v38, v15, v4
	v_lshlrev_b32_e32 v4, 16, v61
	v_fmac_f32_e32 v39, v15, v4
	v_and_b32_e32 v4, 0xffff0000, v61
	v_fmac_f32_e32 v40, v15, v4
	v_lshlrev_b32_e32 v4, 16, v62
	v_fmac_f32_e32 v41, v15, v4
	v_and_b32_e32 v4, 0xffff0000, v62
	v_fmac_f32_e32 v42, v15, v4
	v_lshlrev_b32_e32 v4, 16, v63
	v_fmac_f32_e32 v43, v15, v4
	v_sub_f32_e32 v4, v29, v36
	v_mul_f32_e32 v4, 0x3e38aa3b, v4
	v_fmac_f32_e32 v13, v12, v15
	v_exp_f32_e32 v12, v4
	v_and_b32_e32 v8, 0xffff0000, v63
	v_fmac_f32_e32 v37, v15, v8
	v_fmac_f32_e32 v13, v30, v12
	s_waitcnt lgkmcnt(3)
	v_lshlrev_b32_e32 v15, 16, v64
	v_and_b32_e32 v4, 0xffff0000, v64
	v_fmac_f32_e32 v38, v12, v4
	v_lshlrev_b32_e32 v4, 16, v65
	v_fmac_f32_e32 v39, v12, v4
	v_and_b32_e32 v4, 0xffff0000, v65
	v_sub_f32_e32 v5, v31, v36
	v_fmac_f32_e32 v40, v12, v4
	v_lshlrev_b32_e32 v4, 16, v66
	v_mul_f32_e32 v5, 0x3e38aa3b, v5
	v_fmac_f32_e32 v16, v12, v15
	v_fmac_f32_e32 v41, v12, v4
	v_and_b32_e32 v4, 0xffff0000, v66
	v_exp_f32_e32 v15, v5
	v_fmac_f32_e32 v42, v12, v4
	v_lshlrev_b32_e32 v4, 16, v67
	v_fmac_f32_e32 v43, v12, v4
	v_and_b32_e32 v4, 0xffff0000, v67
	v_fmac_f32_e32 v37, v12, v4
	s_waitcnt lgkmcnt(2)
	v_lshlrev_b32_e32 v4, 16, v68
	v_fmac_f32_e32 v16, v15, v4
	v_and_b32_e32 v4, 0xffff0000, v68
	v_fmac_f32_e32 v38, v15, v4
	v_lshlrev_b32_e32 v4, 16, v69
	v_fmac_f32_e32 v39, v15, v4
	v_and_b32_e32 v4, 0xffff0000, v69
	v_fmac_f32_e32 v40, v15, v4
	v_lshlrev_b32_e32 v4, 16, v70
	v_fmac_f32_e32 v41, v15, v4
	v_and_b32_e32 v4, 0xffff0000, v70
	v_fmac_f32_e32 v42, v15, v4
	v_lshlrev_b32_e32 v4, 16, v71
	v_fmac_f32_e32 v43, v15, v4
	v_sub_f32_e32 v4, v33, v36
	v_mul_f32_e32 v4, 0x3e38aa3b, v4
	v_exp_f32_e32 v12, v4
	v_and_b32_e32 v8, 0xffff0000, v71
	v_fmac_f32_e32 v37, v15, v8
	v_fmac_f32_e32 v13, v32, v15
	s_waitcnt lgkmcnt(1)
	v_lshlrev_b32_e32 v14, 16, v72
	v_and_b32_e32 v4, 0xffff0000, v72
	v_fmac_f32_e32 v38, v12, v4
	v_lshlrev_b32_e32 v4, 16, v73
	v_fmac_f32_e32 v39, v12, v4
	v_and_b32_e32 v4, 0xffff0000, v73
	v_sub_f32_e32 v5, v28, v36
	v_fmac_f32_e32 v40, v12, v4
	v_lshlrev_b32_e32 v4, 16, v74
	v_mul_f32_e32 v5, 0x3e38aa3b, v5
	v_fmac_f32_e32 v41, v12, v4
	v_and_b32_e32 v4, 0xffff0000, v74
	v_exp_f32_e32 v5, v5
	v_fmac_f32_e32 v42, v12, v4
	v_lshlrev_b32_e32 v4, 16, v75
	v_fmac_f32_e32 v43, v12, v4
	v_and_b32_e32 v4, 0xffff0000, v75
	v_fmac_f32_e32 v16, v12, v14
	v_fmac_f32_e32 v37, v12, v4
	s_waitcnt lgkmcnt(0)
	v_lshlrev_b32_e32 v4, 16, v76
	v_fmac_f32_e32 v16, v5, v4
	v_and_b32_e32 v4, 0xffff0000, v76
	v_fmac_f32_e32 v38, v5, v4
	v_lshlrev_b32_e32 v4, 16, v77
	v_fmac_f32_e32 v13, v34, v12
	v_fmac_f32_e32 v39, v5, v4
	v_and_b32_e32 v4, 0xffff0000, v77
	v_fmac_f32_e32 v13, v35, v5
	v_fmac_f32_e32 v40, v5, v4
	v_lshlrev_b32_e32 v4, 16, v78
	v_fmac_f32_e32 v41, v5, v4
	v_and_b32_e32 v4, 0xffff0000, v78
	v_rcp_f32_e32 v6, v13
	v_fmac_f32_e32 v42, v5, v4
	v_lshlrev_b32_e32 v4, 16, v79
	v_fmac_f32_e32 v43, v5, v4
	v_and_b32_e32 v4, 0xffff0000, v79
	v_fmac_f32_e32 v37, v5, v4
	s_waitcnt vmcnt(32)
	v_fmac_f32_e32 v111, v6, v38
	v_fmac_f32_e32 v112, v6, v39
	global_store_dword v118, v111, s[80:81] offset:-4096 nt
	global_store_dword v118, v112, s[80:81] nt
	v_fmac_f32_e32 v117, v6, v40
	global_store_dword v118, v117, s[82:83] nt
	v_fmac_f32_e32 v113, v6, v41
	global_store_dword v118, v113, s[84:85] offset:-4096 nt
	v_fmac_f32_e32 v114, v6, v42
	global_store_dword v118, v114, s[84:85] nt
	v_fmac_f32_e32 v110, v6, v16
	global_store_dword v118, v110, s[14:15] nt
	v_fmac_f32_e32 v115, v6, v43
	v_fmac_f32_e32 v116, v6, v37
	s_and_b64 vcc, exec, s[18:19]
	global_store_dword v118, v115, s[86:87] offset:-4096 nt
	global_store_dword v118, v116, s[86:87] nt
	s_barrier
	s_cbranch_vccnz .LBB3_144
